# main loops regenerated: MFMA/top-2 chain software-pipelined by code tile, output(t) deferred to iteration t+2, merge with fused DPP
# baseline (speedup 1.0000x reference)
.LBB0_81:
	ds_read_b128 v[194:197], v193 offset:4608
	ds_read_b128 v[198:201], v193 offset:4640
	ds_read_b128 v[202:205], v193 offset:4672
	ds_read_b128 v[206:209], v193 offset:4704
	s_min_u32 s6, s5, 11
	v_lshl_add_u32 v66, s6, 13, v191
	v_or_b32_e32 v66, v66, v178
	v_or_b32_e32 v67, 0x1000, v66
	global_load_dwordx4 v[174:177], v66, s[20:21] nt
	global_load_dwordx4 v[170:173], v67, s[20:21] nt
	s_add_i32 s0, s0, 2
	v_add_u32_e32 v192, 0x2400, v192
	v_add_u32_e32 v193, 0x2400, v193
	s_cmp_gt_u32 s5, 13
	s_waitcnt lgkmcnt(3)
	v_mfma_f32_32x32x16_f16 v[66:81], v[98:101], v[194:197], v[2:17]
	s_waitcnt lgkmcnt(2)
	v_mfma_f32_32x32x16_f16 v[66:81], v[102:105], v[198:201], v[66:81]
	s_waitcnt lgkmcnt(1)
	v_mfma_f32_32x32x16_f16 v[66:81], v[106:109], v[202:205], v[66:81]
	s_waitcnt lgkmcnt(0)
	v_mfma_f32_32x32x16_f16 v[66:81], v[110:113], v[206:209], v[66:81]
	v_mfma_f32_32x32x16_f16 v[82:97], v[114:117], v[194:197], v[18:33]
	s_nop 10
	v_and_b32_e32 v66, 0xffffffc0, v66
	v_and_or_b32 v67, v67, s1, 1
	v_and_or_b32 v68, v68, s1, 2
	v_and_or_b32 v69, v69, s1, 3
	v_med3_f32 v212, v66, v67, s4
	v_and_or_b32 v70, v70, s1, 4
	v_min3_f32 v210, v66, s4, v67
	v_and_or_b32 v71, v71, s1, 5
	v_mfma_f32_32x32x16_f16 v[82:97], v[118:121], v[198:201], v[82:97]
	v_med3_f32 v213, v210, v68, v69
	v_and_or_b32 v72, v72, s1, 6
	v_min3_f32 v210, v210, v68, v69
	v_and_or_b32 v73, v73, s1, 7
	v_min3_f32 v211, v212, s4, v213
	v_med3_f32 v212, v210, v70, v71
	v_and_or_b32 v74, v74, s1, 8
	v_min3_f32 v210, v210, v70, v71
	v_mfma_f32_32x32x16_f16 v[82:97], v[122:125], v[202:205], v[82:97]
	v_and_or_b32 v75, v75, s1, 9
	v_med3_f32 v213, v210, v72, v73
	v_and_or_b32 v76, v76, s1, 10
	v_min3_f32 v210, v210, v72, v73
	v_and_or_b32 v77, v77, s1, 11
	v_min3_f32 v211, v211, v212, v213
	v_med3_f32 v212, v210, v74, v75
	v_and_or_b32 v78, v78, s1, 12
	v_mfma_f32_32x32x16_f16 v[82:97], v[126:129], v[206:209], v[82:97]
	v_min3_f32 v210, v210, v74, v75
	v_and_or_b32 v79, v79, s1, 13
	v_med3_f32 v213, v210, v76, v77
	v_and_or_b32 v80, v80, s1, 14
	v_min3_f32 v210, v210, v76, v77
	v_and_or_b32 v81, v81, s1, 15
	v_min3_f32 v211, v211, v212, v213
	v_med3_f32 v212, v210, v78, v79
	v_min3_f32 v210, v210, v78, v79
	v_med3_f32 v213, v210, v80, v81
	v_min3_f32 v210, v210, v80, v81
	v_min3_f32 v211, v211, v212, v213
	v_mfma_f32_32x32x16_f16 v[66:81], v[130:133], v[194:197], v[34:49]
	v_and_or_b32 v82, v82, s1, 16
	v_and_or_b32 v83, v83, s1, 17
	v_and_or_b32 v84, v84, s1, 18
	v_and_or_b32 v85, v85, s1, 19
	v_med3_f32 v212, v210, v82, v83
	v_and_or_b32 v86, v86, s1, 20
	v_min3_f32 v210, v210, v82, v83
	v_and_or_b32 v87, v87, s1, 21
	v_mfma_f32_32x32x16_f16 v[66:81], v[134:137], v[198:201], v[66:81]
	v_med3_f32 v213, v210, v84, v85
	v_and_or_b32 v88, v88, s1, 22
	v_min3_f32 v210, v210, v84, v85
	v_and_or_b32 v89, v89, s1, 23
	v_min3_f32 v211, v211, v212, v213
	v_med3_f32 v212, v210, v86, v87
	v_and_or_b32 v90, v90, s1, 24
	v_min3_f32 v210, v210, v86, v87
	v_mfma_f32_32x32x16_f16 v[66:81], v[138:141], v[202:205], v[66:81]
	v_and_or_b32 v91, v91, s1, 25
	v_med3_f32 v213, v210, v88, v89
	v_and_or_b32 v92, v92, s1, 26
	v_min3_f32 v210, v210, v88, v89
	v_and_or_b32 v93, v93, s1, 27
	v_min3_f32 v211, v211, v212, v213
	v_med3_f32 v212, v210, v90, v91
	v_and_or_b32 v94, v94, s1, 28
	v_mfma_f32_32x32x16_f16 v[66:81], v[142:145], v[206:209], v[66:81]
	v_min3_f32 v210, v210, v90, v91
	v_and_or_b32 v95, v95, s1, 29
	v_med3_f32 v213, v210, v92, v93
	v_and_or_b32 v96, v96, s1, 30
	v_min3_f32 v210, v210, v92, v93
	v_and_or_b32 v97, v97, s1, 31
	v_min3_f32 v211, v211, v212, v213
	v_med3_f32 v212, v210, v94, v95
	v_min3_f32 v210, v210, v94, v95
	v_med3_f32 v213, v210, v96, v97
	v_min3_f32 v210, v210, v96, v97
	v_min3_f32 v211, v211, v212, v213
	v_mfma_f32_32x32x16_f16 v[82:97], v[146:149], v[194:197], v[50:65]
	v_and_or_b32 v66, v66, s1, 32
	v_and_or_b32 v67, v67, s1, 33
	v_and_or_b32 v68, v68, s1, 34
	v_and_or_b32 v69, v69, s1, 35
	v_med3_f32 v212, v210, v66, v67
	v_and_or_b32 v70, v70, s1, 36
	v_min3_f32 v210, v210, v66, v67
	v_and_or_b32 v71, v71, s1, 37
	v_mfma_f32_32x32x16_f16 v[82:97], v[150:153], v[198:201], v[82:97]
	v_med3_f32 v213, v210, v68, v69
	v_and_or_b32 v72, v72, s1, 38
	v_min3_f32 v210, v210, v68, v69
	v_and_or_b32 v73, v73, s1, 39
	v_min3_f32 v211, v211, v212, v213
	v_med3_f32 v212, v210, v70, v71
	v_and_or_b32 v74, v74, s1, 40
	v_min3_f32 v210, v210, v70, v71
	v_mfma_f32_32x32x16_f16 v[82:97], v[154:157], v[202:205], v[82:97]
	v_and_or_b32 v75, v75, s1, 41
	v_med3_f32 v213, v210, v72, v73
	v_and_or_b32 v76, v76, s1, 42
	v_min3_f32 v210, v210, v72, v73
	v_and_or_b32 v77, v77, s1, 43
	v_min3_f32 v211, v211, v212, v213
	v_med3_f32 v212, v210, v74, v75
	v_and_or_b32 v78, v78, s1, 44
	v_mfma_f32_32x32x16_f16 v[82:97], v[158:161], v[206:209], v[82:97]
	v_min3_f32 v210, v210, v74, v75
	v_and_or_b32 v79, v79, s1, 45
	v_med3_f32 v213, v210, v76, v77
	v_and_or_b32 v80, v80, s1, 46
	v_min3_f32 v210, v210, v76, v77
	v_and_or_b32 v81, v81, s1, 47
	v_min3_f32 v211, v211, v212, v213
	v_med3_f32 v212, v210, v78, v79
	v_min3_f32 v210, v210, v78, v79
	v_med3_f32 v213, v210, v80, v81
	v_min3_f32 v210, v210, v80, v81
	v_min3_f32 v211, v211, v212, v213
	v_and_or_b32 v82, v82, s1, 48
	v_and_or_b32 v83, v83, s1, 49
	v_and_or_b32 v84, v84, s1, 50
	v_and_or_b32 v85, v85, s1, 51
	v_med3_f32 v212, v210, v82, v83
	v_and_or_b32 v86, v86, s1, 52
	v_min3_f32 v210, v210, v82, v83
	v_and_or_b32 v87, v87, s1, 53
	v_med3_f32 v213, v210, v84, v85
	v_and_or_b32 v88, v88, s1, 54
	v_min3_f32 v210, v210, v84, v85
	v_and_or_b32 v89, v89, s1, 55
	v_min3_f32 v211, v211, v212, v213
	v_med3_f32 v212, v210, v86, v87
	v_and_or_b32 v90, v90, s1, 56
	v_min3_f32 v210, v210, v86, v87
	v_and_or_b32 v91, v91, s1, 57
	v_med3_f32 v213, v210, v88, v89
	v_and_or_b32 v92, v92, s1, 58
	v_min3_f32 v210, v210, v88, v89
	v_and_or_b32 v93, v93, s1, 59
	v_min3_f32 v211, v211, v212, v213
	v_med3_f32 v212, v210, v90, v91
	v_and_or_b32 v94, v94, s1, 60
	v_min3_f32 v210, v210, v90, v91
	v_and_or_b32 v95, v95, s1, 61
	v_med3_f32 v213, v210, v92, v93
	v_and_or_b32 v96, v96, s1, 62
	v_min3_f32 v210, v210, v92, v93
	v_or_b32_e32 v97, 63, v97
	v_min3_f32 v211, v211, v212, v213
	v_med3_f32 v212, v210, v94, v95
	v_min3_f32 v210, v210, v94, v95
	v_med3_f32 v213, v210, v96, v97
	v_min3_f32 v210, v210, v96, v97
	v_min3_f32 v211, v211, v212, v213
	ds_write_b64 v189, v[210:211] offset:4608
	s_waitcnt lgkmcnt(0)
	s_barrier
	s_cbranch_scc1 .LBB0_84
.LBB0_82:
	s_waitcnt vmcnt(3)
	v_cvt_pk_f16_f32 v67, v168, v169
	v_cvt_pk_f16_f32 v66, v166, v167
	ds_write_b64 v192, v[66:67]
	s_waitcnt vmcnt(2)
	v_cvt_pk_f16_f32 v67, v164, v165
	v_cvt_pk_f16_f32 v66, v162, v163
	ds_write_b64 v192, v[66:67] offset:2304
	ds_read_b128 v[194:197], v193
	ds_read_b128 v[198:201], v193 offset:32
	ds_read_b128 v[202:205], v193 offset:64
	ds_read_b128 v[206:209], v193 offset:96
	s_add_i32 s6, s0, -1
	s_add_i32 s5, s0, -2
	s_and_b32 s6, s6, 3
	s_min_u32 s7, s5, 12
	s_lshl_b32 s6, s6, 13
	v_lshl_add_u32 v66, s7, 13, v190
	s_add_i32 s6, s6, 0x12000
	v_or_b32_e32 v66, v66, v178
	v_lshl_or_b32 v67, v187, 4, s6
	v_lshl_or_b32 v84, v188, 4, s6
	v_or_b32_e32 v85, 0x1000, v66
	ds_write_b128 v67, v[166:169]
	ds_write_b128 v84, v[162:165]
	global_load_dwordx4 v[166:169], v66, s[20:21] nt
	global_load_dwordx4 v[162:165], v85, s[20:21] nt
	s_cmp_gt_u32 s5, 13
	s_waitcnt lgkmcnt(5)
	v_mfma_f32_32x32x16_f16 v[66:81], v[98:101], v[194:197], v[2:17]
	s_waitcnt lgkmcnt(4)
	v_mfma_f32_32x32x16_f16 v[66:81], v[102:105], v[198:201], v[66:81]
	s_waitcnt lgkmcnt(3)
	v_mfma_f32_32x32x16_f16 v[66:81], v[106:109], v[202:205], v[66:81]
	s_waitcnt lgkmcnt(2)
	v_mfma_f32_32x32x16_f16 v[66:81], v[110:113], v[206:209], v[66:81]
	v_mfma_f32_32x32x16_f16 v[82:97], v[114:117], v[194:197], v[18:33]
	s_nop 10
	v_and_b32_e32 v66, 0xffffffc0, v66
	v_and_or_b32 v67, v67, s1, 1
	v_and_or_b32 v68, v68, s1, 2
	v_and_or_b32 v69, v69, s1, 3
	v_med3_f32 v212, v66, v67, s4
	v_and_or_b32 v70, v70, s1, 4
	v_min3_f32 v210, v66, s4, v67
	v_and_or_b32 v71, v71, s1, 5
	v_mfma_f32_32x32x16_f16 v[82:97], v[118:121], v[198:201], v[82:97]
	v_med3_f32 v213, v210, v68, v69
	v_and_or_b32 v72, v72, s1, 6
	v_min3_f32 v210, v210, v68, v69
	v_and_or_b32 v73, v73, s1, 7
	v_min3_f32 v211, v212, s4, v213
	v_med3_f32 v212, v210, v70, v71
	v_and_or_b32 v74, v74, s1, 8
	v_min3_f32 v210, v210, v70, v71
	v_mfma_f32_32x32x16_f16 v[82:97], v[122:125], v[202:205], v[82:97]
	v_and_or_b32 v75, v75, s1, 9
	v_med3_f32 v213, v210, v72, v73
	v_and_or_b32 v76, v76, s1, 10
	v_min3_f32 v210, v210, v72, v73
	v_and_or_b32 v77, v77, s1, 11
	v_min3_f32 v211, v211, v212, v213
	v_med3_f32 v212, v210, v74, v75
	v_and_or_b32 v78, v78, s1, 12
	v_mfma_f32_32x32x16_f16 v[82:97], v[126:129], v[206:209], v[82:97]
	v_min3_f32 v210, v210, v74, v75
	v_and_or_b32 v79, v79, s1, 13
	v_med3_f32 v213, v210, v76, v77
	v_and_or_b32 v80, v80, s1, 14
	v_min3_f32 v210, v210, v76, v77
	v_and_or_b32 v81, v81, s1, 15
	v_min3_f32 v211, v211, v212, v213
	v_med3_f32 v212, v210, v78, v79
	v_min3_f32 v210, v210, v78, v79
	v_med3_f32 v213, v210, v80, v81
	v_min3_f32 v210, v210, v80, v81
	v_min3_f32 v211, v211, v212, v213
	v_mfma_f32_32x32x16_f16 v[66:81], v[130:133], v[194:197], v[34:49]
	v_and_or_b32 v82, v82, s1, 16
	v_and_or_b32 v83, v83, s1, 17
	v_and_or_b32 v84, v84, s1, 18
	v_and_or_b32 v85, v85, s1, 19
	v_med3_f32 v212, v210, v82, v83
	v_and_or_b32 v86, v86, s1, 20
	v_min3_f32 v210, v210, v82, v83
	v_and_or_b32 v87, v87, s1, 21
	v_mfma_f32_32x32x16_f16 v[66:81], v[134:137], v[198:201], v[66:81]
	v_med3_f32 v213, v210, v84, v85
	v_and_or_b32 v88, v88, s1, 22
	v_min3_f32 v210, v210, v84, v85
	v_and_or_b32 v89, v89, s1, 23
	v_min3_f32 v211, v211, v212, v213
	v_med3_f32 v212, v210, v86, v87
	v_and_or_b32 v90, v90, s1, 24
	v_min3_f32 v210, v210, v86, v87
	v_mfma_f32_32x32x16_f16 v[66:81], v[138:141], v[202:205], v[66:81]
	v_and_or_b32 v91, v91, s1, 25
	v_med3_f32 v213, v210, v88, v89
	v_and_or_b32 v92, v92, s1, 26
	v_min3_f32 v210, v210, v88, v89
	v_and_or_b32 v93, v93, s1, 27
	v_min3_f32 v211, v211, v212, v213
	v_med3_f32 v212, v210, v90, v91
	v_and_or_b32 v94, v94, s1, 28
	v_mfma_f32_32x32x16_f16 v[66:81], v[142:145], v[206:209], v[66:81]
	v_min3_f32 v210, v210, v90, v91
	v_and_or_b32 v95, v95, s1, 29
	v_med3_f32 v213, v210, v92, v93
	v_and_or_b32 v96, v96, s1, 30
	v_min3_f32 v210, v210, v92, v93
	v_and_or_b32 v97, v97, s1, 31
	v_min3_f32 v211, v211, v212, v213
	v_med3_f32 v212, v210, v94, v95
	v_min3_f32 v210, v210, v94, v95
	v_med3_f32 v213, v210, v96, v97
	v_min3_f32 v210, v210, v96, v97
	v_min3_f32 v211, v211, v212, v213
	v_mfma_f32_32x32x16_f16 v[82:97], v[146:149], v[194:197], v[50:65]
	v_and_or_b32 v66, v66, s1, 32
	v_and_or_b32 v67, v67, s1, 33
	v_and_or_b32 v68, v68, s1, 34
	v_and_or_b32 v69, v69, s1, 35
	v_med3_f32 v212, v210, v66, v67
	v_and_or_b32 v70, v70, s1, 36
	v_min3_f32 v210, v210, v66, v67
	v_and_or_b32 v71, v71, s1, 37
	v_mfma_f32_32x32x16_f16 v[82:97], v[150:153], v[198:201], v[82:97]
	v_med3_f32 v213, v210, v68, v69
	v_and_or_b32 v72, v72, s1, 38
	v_min3_f32 v210, v210, v68, v69
	v_and_or_b32 v73, v73, s1, 39
	v_min3_f32 v211, v211, v212, v213
	v_med3_f32 v212, v210, v70, v71
	v_and_or_b32 v74, v74, s1, 40
	v_min3_f32 v210, v210, v70, v71
	v_mfma_f32_32x32x16_f16 v[82:97], v[154:157], v[202:205], v[82:97]
	v_and_or_b32 v75, v75, s1, 41
	v_med3_f32 v213, v210, v72, v73
	v_and_or_b32 v76, v76, s1, 42
	v_min3_f32 v210, v210, v72, v73
	v_and_or_b32 v77, v77, s1, 43
	v_min3_f32 v211, v211, v212, v213
	v_med3_f32 v212, v210, v74, v75
	v_and_or_b32 v78, v78, s1, 44
	v_mfma_f32_32x32x16_f16 v[82:97], v[158:161], v[206:209], v[82:97]
	v_min3_f32 v210, v210, v74, v75
	v_and_or_b32 v79, v79, s1, 45
	v_med3_f32 v213, v210, v76, v77
	v_and_or_b32 v80, v80, s1, 46
	v_min3_f32 v210, v210, v76, v77
	v_and_or_b32 v81, v81, s1, 47
	v_min3_f32 v211, v211, v212, v213
	v_med3_f32 v212, v210, v78, v79
	v_min3_f32 v210, v210, v78, v79
	v_med3_f32 v213, v210, v80, v81
	v_min3_f32 v210, v210, v80, v81
	v_min3_f32 v211, v211, v212, v213
	v_and_or_b32 v82, v82, s1, 48
	v_and_or_b32 v83, v83, s1, 49
	v_and_or_b32 v84, v84, s1, 50
	v_and_or_b32 v85, v85, s1, 51
	v_med3_f32 v212, v210, v82, v83
	v_and_or_b32 v86, v86, s1, 52
	v_min3_f32 v210, v210, v82, v83
	v_and_or_b32 v87, v87, s1, 53
	v_med3_f32 v213, v210, v84, v85
	v_and_or_b32 v88, v88, s1, 54
	v_min3_f32 v210, v210, v84, v85
	v_and_or_b32 v89, v89, s1, 55
	v_min3_f32 v211, v211, v212, v213
	v_med3_f32 v212, v210, v86, v87
	v_and_or_b32 v90, v90, s1, 56
	v_min3_f32 v210, v210, v86, v87
	v_and_or_b32 v91, v91, s1, 57
	v_med3_f32 v213, v210, v88, v89
	v_and_or_b32 v92, v92, s1, 58
	v_min3_f32 v210, v210, v88, v89
	v_and_or_b32 v93, v93, s1, 59
	v_min3_f32 v211, v211, v212, v213
	v_med3_f32 v212, v210, v90, v91
	v_and_or_b32 v94, v94, s1, 60
	v_min3_f32 v210, v210, v90, v91
	v_and_or_b32 v95, v95, s1, 61
	v_med3_f32 v213, v210, v92, v93
	v_and_or_b32 v96, v96, s1, 62
	v_min3_f32 v210, v210, v92, v93
	v_or_b32_e32 v97, 63, v97
	v_min3_f32 v211, v211, v212, v213
	v_med3_f32 v212, v210, v94, v95
	v_min3_f32 v210, v210, v94, v95
	v_med3_f32 v213, v210, v96, v97
	v_min3_f32 v210, v210, v96, v97
	v_min3_f32 v211, v211, v212, v213
	ds_write_b64 v189, v[210:211]
	s_waitcnt lgkmcnt(0)
	s_barrier
	s_cbranch_scc1 .LBB0_81
	s_and_b32 s6, s0, 2
	s_waitcnt vmcnt(3)
	v_cvt_pk_f16_f32 v67, v176, v177
	v_cvt_pk_f16_f32 v66, v174, v175
	s_lshl_b32 s6, s6, 13
	ds_write_b64 v192, v[66:67] offset:4608
	s_waitcnt vmcnt(2)
	v_cvt_pk_f16_f32 v67, v172, v173
	v_cvt_pk_f16_f32 v66, v170, v171
	s_or_b32 s6, s6, 0x12000
	ds_write_b64 v192, v[66:67] offset:6912
	v_lshl_or_b32 v66, v187, 4, s6
	ds_write_b128 v66, v[174:177]
	v_lshl_or_b32 v66, v188, 4, s6
	ds_write_b128 v66, v[170:173]
	s_branch .LBB0_81

.LBB0_87:
	s_waitcnt lgkmcnt(0)
	s_barrier
	s_add_i32 s17, s17, 1
	v_add_u32_e32 v179, 0x1200, v179
	v_add_u32_e32 v188, 0x80, v188
	v_add_u32_e32 v186, 0x80, v186
	s_cmp_lg_u32 s17, 16
	v_add_u32_e32 v166, 32, v166
	s_cbranch_scc0 .LBB0_97
.LBB0_88:
	s_add_i32 s29, s17, -1
	s_and_b32 s0, s29, 1
	s_mulk_i32 s0, 0x1200
	v_add_u32_e32 v254, s0, v185
	ds_read_b128 v[250:253], v254
	s_add_i32 s1, s17, -2
	s_and_b32 s1, s1, 3
	v_lshl_add_u32 v66, s1, 13, v175
	v_lshl_add_u32 v67, s1, 13, v174
	ds_read_b128 v[82:85], v66
	ds_read_b128 v[86:89], v67
	ds_read_b128 v[194:197], v179
	ds_read_b128 v[198:201], v179 offset:32
	ds_read_b128 v[202:205], v179 offset:64
	ds_read_b128 v[206:209], v179 offset:96
	s_cmp_lt_u32 s17, 2
	s_cbranch_scc1 .Low_noout
	v_cmp_lt_i32_e64 s[0:1], -1, v192
	s_waitcnt vmcnt(0) lgkmcnt(4)
	s_and_saveexec_b64 s[6:7], s[0:1]
	s_cbranch_execz .Low_a_donel
	v_pk_add_f32 v[66:67], v[246:247], v[82:83] neg_lo:[0,1] neg_hi:[0,1]
	v_pk_add_f32 v[74:75], v[248:249], v[84:85] neg_lo:[0,1] neg_hi:[0,1]
	v_pk_mul_f32 v[76:77], v[66:67], v[66:67]
	v_pk_add_f32 v[66:67], v[82:83], v[66:67]
	v_pk_add_f32 v[68:69], v[84:85], v[74:75]
	v_pk_mul_f32 v[70:71], v[74:75], v[74:75]
	global_store_dwordx4 v[168:169], v[66:69], off sc0 sc1
	s_nop 1
	v_add_f32_e32 v66, v76, v77
	v_add_f32_e32 v66, v66, v70
	v_add_f32_e32 v66, v66, v71
	v_add_f32_e32 v167, v167, v66
.Low_a_donel:
	s_or_b64 exec, exec, s[6:7]
	v_cmp_lt_i32_e64 s[0:1], -1, v191
	s_and_saveexec_b64 s[6:7], s[0:1]
	s_cbranch_execz .Low_b_donel
	v_pk_add_f32 v[70:71], v[162:163], v[86:87] neg_lo:[0,1] neg_hi:[0,1]
	v_pk_add_f32 v[72:73], v[164:165], v[88:89] neg_lo:[0,1] neg_hi:[0,1]
	v_pk_mul_f32 v[74:75], v[70:71], v[70:71]
	v_pk_add_f32 v[66:67], v[86:87], v[70:71]
	v_pk_add_f32 v[68:69], v[88:89], v[72:73]
	v_pk_mul_f32 v[70:71], v[72:73], v[72:73]
	global_store_dwordx4 v[170:171], v[66:69], off sc0 sc1
	s_nop 1
	v_add_f32_e32 v66, v74, v75
	v_add_f32_e32 v66, v66, v70
	v_add_f32_e32 v66, v66, v71
	v_add_f32_e32 v167, v167, v66
.Low_b_donel:
	s_or_b64 exec, exec, s[6:7]
	v_lshl_add_u64 v[168:169], v[168:169], 0, s[4:5]
	v_lshl_add_u64 v[170:171], v[170:171], 0, s[4:5]
.Low_noout:
	s_waitcnt lgkmcnt(6)
	v_lshlrev_b32_e32 v210, 1, v250
	v_lshlrev_b32_e32 v211, 1, v252
	v_and_b32_e32 v212, 0xfffffc03, v250
	v_and_b32_e32 v213, 0xfffffc03, v252
	v_and_b32_e32 v210, 0x78, v210
	v_and_b32_e32 v211, 0x78, v211
	v_or3_b32 v212, v212, v210, v176
	v_or3_b32 v213, v213, v211, v187
	v_min_f32_e32 v210, v212, v213
	v_max_f32_e32 v211, v212, v213
	v_min3_f32 v211, v251, v253, v211
	v_max_f32_dpp v212, v210, v210 quad_perm:[1,0,3,2] row_mask:0xf bank_mask:0xf
	v_min_f32_dpp v213, v210, v210 quad_perm:[1,0,3,2] row_mask:0xf bank_mask:0xf
	v_mov_b32_dpp v254, v211 quad_perm:[1,0,3,2] row_mask:0xf bank_mask:0xf
	v_min3_f32 v211, v211, v254, v212
	v_max_f32_dpp v212, v213, v213 quad_perm:[2,3,0,1] row_mask:0xf bank_mask:0xf
	v_min_f32_dpp v210, v213, v213 quad_perm:[2,3,0,1] row_mask:0xf bank_mask:0xf
	v_mov_b32_dpp v254, v211 quad_perm:[2,3,0,1] row_mask:0xf bank_mask:0xf
	v_min3_f32 v211, v211, v254, v212
	v_max_f32_dpp v212, v210, v210 row_half_mirror row_mask:0xf bank_mask:0xf
	v_min_f32_dpp v213, v210, v210 row_half_mirror row_mask:0xf bank_mask:0xf
	v_mov_b32_dpp v254, v211 row_half_mirror row_mask:0xf bank_mask:0xf
	v_min3_f32 v211, v211, v254, v212
	s_and_saveexec_b64 s[6:7], vcc
	s_cbranch_execz .Low_m_done
	v_sub_f32_e32 v212, v211, v213
	v_cmp_gt_f32_e64 s[0:1], s26, v212
	s_nop 1
	v_cndmask_b32_e64 v212, 0, v190, s[0:1]
	v_and_or_b32 v212, v213, s27, v212
	ds_write_b32 v186, v212
	s_and_b64 exec, exec, s[0:1]
	s_cbranch_execz .Low_m_done
	s_mov_b64 s[14:15], exec
	v_mbcnt_lo_u32_b32 v212, s14, 0
	v_mbcnt_hi_u32_b32 v212, s15, v212
	v_cmp_eq_u32_e64 s[0:1], 0, v212
	s_and_saveexec_b64 s[8:9], s[0:1]
	s_bcnt1_i32_b64 s0, s[14:15]
	v_mov_b32_e32 v254, s0
	ds_add_rtn_u32 v254, v189, v254
	s_or_b64 exec, exec, s[8:9]
	s_waitcnt lgkmcnt(0)
	v_readfirstlane_b32 s0, v254
	v_add_f32_e32 v213, 0x3dcccccd, v213
	s_nop 0
	v_add_lshl_u32 v212, s0, v212, 2
	v_add_u32_e32 v254, 0x21400, v212
	v_add_u32_e32 v212, 0x20400, v212
	ds_write_b32 v254, v166
	ds_write_b32 v212, v213
.Low_m_done:
	s_or_b64 exec, exec, s[6:7]
	s_waitcnt lgkmcnt(0)
	v_mfma_f32_32x32x16_f16 v[66:81], v[98:101], v[194:197], v[2:17]
	v_mfma_f32_32x32x16_f16 v[66:81], v[102:105], v[198:201], v[66:81]
	v_add_u32_e32 v254, 0x20c00, v188
	s_waitcnt lgkmcnt(0)
	ds_read_b32 v191, v254 offset:64
	ds_read_b32 v192, v254
	v_mfma_f32_32x32x16_f16 v[66:81], v[106:109], v[202:205], v[66:81]
	v_mfma_f32_32x32x16_f16 v[66:81], v[110:113], v[206:209], v[66:81]
	v_mfma_f32_32x32x16_f16 v[82:97], v[114:117], v[194:197], v[18:33]
	s_waitcnt lgkmcnt(0)
	v_lshlrev_b32_e32 v212, 4, v191
	v_and_or_b32 v212, v212, s28, v1
	v_lshlrev_b32_e32 v212, 4, v212
	global_load_dwordx4 v[162:165], v212, s[22:23]
	v_lshlrev_b32_e32 v213, 4, v192
	v_and_or_b32 v213, v213, s28, v1
	v_lshlrev_b32_e32 v213, 4, v213
	global_load_dwordx4 v[246:249], v213, s[22:23]
	s_nop 1
	v_and_b32_e32 v66, 0xffffffc0, v66
	v_and_or_b32 v67, v67, s16, 1
	v_and_or_b32 v68, v68, s16, 2
	v_and_or_b32 v69, v69, s16, 3
	v_med3_f32 v212, v66, v67, s25
	v_and_or_b32 v70, v70, s16, 4
	v_min3_f32 v210, v66, s25, v67
	v_and_or_b32 v71, v71, s16, 5
	v_mfma_f32_32x32x16_f16 v[82:97], v[118:121], v[198:201], v[82:97]
	v_med3_f32 v213, v210, v68, v69
	v_and_or_b32 v72, v72, s16, 6
	v_min3_f32 v210, v210, v68, v69
	v_and_or_b32 v73, v73, s16, 7
	v_min3_f32 v211, v212, s25, v213
	v_med3_f32 v212, v210, v70, v71
	v_and_or_b32 v74, v74, s16, 8
	v_min3_f32 v210, v210, v70, v71
	v_mfma_f32_32x32x16_f16 v[82:97], v[122:125], v[202:205], v[82:97]
	v_and_or_b32 v75, v75, s16, 9
	v_med3_f32 v213, v210, v72, v73
	v_and_or_b32 v76, v76, s16, 10
	v_min3_f32 v210, v210, v72, v73
	v_and_or_b32 v77, v77, s16, 11
	v_min3_f32 v211, v211, v212, v213
	v_med3_f32 v212, v210, v74, v75
	v_and_or_b32 v78, v78, s16, 12
	v_mfma_f32_32x32x16_f16 v[82:97], v[126:129], v[206:209], v[82:97]
	v_min3_f32 v210, v210, v74, v75
	v_and_or_b32 v79, v79, s16, 13
	v_med3_f32 v213, v210, v76, v77
	v_and_or_b32 v80, v80, s16, 14
	v_min3_f32 v210, v210, v76, v77
	v_and_or_b32 v81, v81, s16, 15
	v_min3_f32 v211, v211, v212, v213
	v_med3_f32 v212, v210, v78, v79
	v_min3_f32 v210, v210, v78, v79
	v_med3_f32 v213, v210, v80, v81
	v_min3_f32 v210, v210, v80, v81
	v_min3_f32 v211, v211, v212, v213
	v_mfma_f32_32x32x16_f16 v[66:81], v[130:133], v[194:197], v[34:49]
	v_and_or_b32 v82, v82, s16, 16
	v_and_or_b32 v83, v83, s16, 17
	v_and_or_b32 v84, v84, s16, 18
	v_and_or_b32 v85, v85, s16, 19
	v_med3_f32 v212, v210, v82, v83
	v_and_or_b32 v86, v86, s16, 20
	v_min3_f32 v210, v210, v82, v83
	v_and_or_b32 v87, v87, s16, 21
	v_mfma_f32_32x32x16_f16 v[66:81], v[134:137], v[198:201], v[66:81]
	v_med3_f32 v213, v210, v84, v85
	v_and_or_b32 v88, v88, s16, 22
	v_min3_f32 v210, v210, v84, v85
	v_and_or_b32 v89, v89, s16, 23
	v_min3_f32 v211, v211, v212, v213
	v_med3_f32 v212, v210, v86, v87
	v_and_or_b32 v90, v90, s16, 24
	v_min3_f32 v210, v210, v86, v87
	v_mfma_f32_32x32x16_f16 v[66:81], v[138:141], v[202:205], v[66:81]
	v_and_or_b32 v91, v91, s16, 25
	v_med3_f32 v213, v210, v88, v89
	v_and_or_b32 v92, v92, s16, 26
	v_min3_f32 v210, v210, v88, v89
	v_and_or_b32 v93, v93, s16, 27
	v_min3_f32 v211, v211, v212, v213
	v_med3_f32 v212, v210, v90, v91
	v_and_or_b32 v94, v94, s16, 28
	v_mfma_f32_32x32x16_f16 v[66:81], v[142:145], v[206:209], v[66:81]
	v_min3_f32 v210, v210, v90, v91
	v_and_or_b32 v95, v95, s16, 29
	v_med3_f32 v213, v210, v92, v93
	v_and_or_b32 v96, v96, s16, 30
	v_min3_f32 v210, v210, v92, v93
	v_and_or_b32 v97, v97, s16, 31
	v_min3_f32 v211, v211, v212, v213
	v_med3_f32 v212, v210, v94, v95
	v_min3_f32 v210, v210, v94, v95
	v_med3_f32 v213, v210, v96, v97
	v_min3_f32 v210, v210, v96, v97
	v_min3_f32 v211, v211, v212, v213
	v_mfma_f32_32x32x16_f16 v[82:97], v[146:149], v[194:197], v[50:65]
	v_and_or_b32 v66, v66, s16, 32
	v_and_or_b32 v67, v67, s16, 33
	v_and_or_b32 v68, v68, s16, 34
	v_and_or_b32 v69, v69, s16, 35
	v_med3_f32 v212, v210, v66, v67
	v_and_or_b32 v70, v70, s16, 36
	v_min3_f32 v210, v210, v66, v67
	v_and_or_b32 v71, v71, s16, 37
	v_mfma_f32_32x32x16_f16 v[82:97], v[150:153], v[198:201], v[82:97]
	v_med3_f32 v213, v210, v68, v69
	v_and_or_b32 v72, v72, s16, 38
	v_min3_f32 v210, v210, v68, v69
	v_and_or_b32 v73, v73, s16, 39
	v_min3_f32 v211, v211, v212, v213
	v_med3_f32 v212, v210, v70, v71
	v_and_or_b32 v74, v74, s16, 40
	v_min3_f32 v210, v210, v70, v71
	v_mfma_f32_32x32x16_f16 v[82:97], v[154:157], v[202:205], v[82:97]
	v_and_or_b32 v75, v75, s16, 41
	v_med3_f32 v213, v210, v72, v73
	v_and_or_b32 v76, v76, s16, 42
	v_min3_f32 v210, v210, v72, v73
	v_and_or_b32 v77, v77, s16, 43
	v_min3_f32 v211, v211, v212, v213
	v_med3_f32 v212, v210, v74, v75
	v_and_or_b32 v78, v78, s16, 44
	v_mfma_f32_32x32x16_f16 v[82:97], v[158:161], v[206:209], v[82:97]
	v_min3_f32 v210, v210, v74, v75
	v_and_or_b32 v79, v79, s16, 45
	v_med3_f32 v213, v210, v76, v77
	v_and_or_b32 v80, v80, s16, 46
	v_min3_f32 v210, v210, v76, v77
	v_and_or_b32 v81, v81, s16, 47
	v_min3_f32 v211, v211, v212, v213
	v_med3_f32 v212, v210, v78, v79
	v_min3_f32 v210, v210, v78, v79
	v_med3_f32 v213, v210, v80, v81
	v_min3_f32 v210, v210, v80, v81
	v_min3_f32 v211, v211, v212, v213
	v_and_or_b32 v82, v82, s16, 48
	v_and_or_b32 v83, v83, s16, 49
	v_and_or_b32 v84, v84, s16, 50
	v_and_or_b32 v85, v85, s16, 51
	v_med3_f32 v212, v210, v82, v83
	v_and_or_b32 v86, v86, s16, 52
	v_min3_f32 v210, v210, v82, v83
	v_and_or_b32 v87, v87, s16, 53
	v_med3_f32 v213, v210, v84, v85
	v_and_or_b32 v88, v88, s16, 54
	v_min3_f32 v210, v210, v84, v85
	v_and_or_b32 v89, v89, s16, 55
	v_min3_f32 v211, v211, v212, v213
	v_med3_f32 v212, v210, v86, v87
	v_and_or_b32 v90, v90, s16, 56
	v_min3_f32 v210, v210, v86, v87
	v_and_or_b32 v91, v91, s16, 57
	v_med3_f32 v213, v210, v88, v89
	v_and_or_b32 v92, v92, s16, 58
	v_min3_f32 v210, v210, v88, v89
	v_and_or_b32 v93, v93, s16, 59
	v_min3_f32 v211, v211, v212, v213
	v_med3_f32 v212, v210, v90, v91
	v_and_or_b32 v94, v94, s16, 60
	v_min3_f32 v210, v210, v90, v91
	v_and_or_b32 v95, v95, s16, 61
	v_med3_f32 v213, v210, v92, v93
	v_and_or_b32 v96, v96, s16, 62
	v_min3_f32 v210, v210, v92, v93
	v_or_b32_e32 v97, 63, v97
	v_min3_f32 v211, v211, v212, v213
	v_med3_f32 v212, v210, v94, v95
	v_min3_f32 v210, v210, v94, v95
	v_med3_f32 v213, v210, v96, v97
	v_min3_f32 v210, v210, v96, v97
	v_min3_f32 v211, v211, v212, v213
	s_and_b32 s0, s17, 1
	s_mulk_i32 s0, 0x1200
	v_add_u32_e32 v254, s0, v177
	ds_write_b64 v254, v[210:211]
	s_branch .LBB0_87
.LBB0_97:
	s_add_i32 s1, s17, -2
	s_and_b32 s1, s1, 3
	v_lshl_add_u32 v66, s1, 13, v175
	v_lshl_add_u32 v67, s1, 13, v174
	ds_read_b128 v[82:85], v66
	ds_read_b128 v[86:89], v67
	v_cmp_lt_i32_e64 s[0:1], -1, v192
	s_waitcnt vmcnt(0) lgkmcnt(0)
	s_and_saveexec_b64 s[6:7], s[0:1]
	s_cbranch_execz .Low_a_doned
	v_pk_add_f32 v[66:67], v[246:247], v[82:83] neg_lo:[0,1] neg_hi:[0,1]
	v_pk_add_f32 v[74:75], v[248:249], v[84:85] neg_lo:[0,1] neg_hi:[0,1]
	v_pk_mul_f32 v[76:77], v[66:67], v[66:67]
	v_pk_add_f32 v[66:67], v[82:83], v[66:67]
	v_pk_add_f32 v[68:69], v[84:85], v[74:75]
	v_pk_mul_f32 v[70:71], v[74:75], v[74:75]
	global_store_dwordx4 v[168:169], v[66:69], off sc0 sc1
	s_nop 1
	v_add_f32_e32 v66, v76, v77
	v_add_f32_e32 v66, v66, v70
	v_add_f32_e32 v66, v66, v71
	v_add_f32_e32 v167, v167, v66

.Low_b_doned:
	s_or_b64 exec, exec, s[6:7]
	ds_read_b128 v[66:69], v185 offset:4608
	s_movk_i32 s0, 0xfc03
	s_waitcnt lgkmcnt(0)
	v_lshlrev_b32_e32 v71, 1, v68
	v_lshlrev_b32_e32 v70, 1, v66
	v_and_b32_e32 v71, 0x78, v71
	v_and_b32_e32 v66, 0xfffffc03, v66
	v_and_b32_e32 v70, 0x78, v70
	v_and_or_b32 v68, v68, s0, v71
	v_or3_b32 v66, v66, v70, v176
	v_or3_b32 v68, v68, v176, 4
	v_max_f32_e32 v66, v66, v66
	v_max_f32_e32 v68, v68, v68
	v_min_f32_e32 v70, v66, v68
	v_max_f32_e32 v66, v66, v68
	v_mov_b32_e32 v68, 0
	v_min3_f32 v66, v67, v69, v66
	v_mov_b32_e32 v69, 0
	v_mov_b32_dpp v68, v70 quad_perm:[1,0,3,2] row_mask:0xf bank_mask:0xf
	v_max_f32_e32 v68, v68, v68
	v_mov_b32_dpp v69, v66 quad_perm:[1,0,3,2] row_mask:0xf bank_mask:0xf
	v_max_f32_e32 v71, v70, v68
	v_min3_f32 v66, v66, v69, v71
	v_min_f32_e32 v69, v70, v68
	v_mov_b32_e32 v68, 0
	v_mov_b32_e32 v70, 0
	v_mov_b32_e32 v67, 0
	v_mov_b32_dpp v68, v69 quad_perm:[2,3,0,1] row_mask:0xf bank_mask:0xf
	v_max_f32_e32 v71, v68, v68
	v_mov_b32_dpp v70, v66 quad_perm:[2,3,0,1] row_mask:0xf bank_mask:0xf
	v_max_f32_e32 v68, v69, v71
	v_min3_f32 v68, v66, v70, v68
	v_min_f32_e32 v66, v69, v71
	v_mov_b32_e32 v69, 0
	v_mov_b32_dpp v67, v68 row_half_mirror row_mask:0xf bank_mask:0xf
	s_nop 0
	v_mov_b32_dpp v69, v66 row_half_mirror row_mask:0xf bank_mask:0xf
	s_and_saveexec_b64 s[0:1], vcc
	s_cbranch_execz .LBB0_102
	v_max_f32_e32 v69, v69, v69
	v_max_f32_e32 v70, v66, v66
	v_min_f32_e32 v66, v70, v69
	v_max_f32_e32 v69, v70, v69
	v_min3_f32 v67, v68, v67, v69
	v_sub_f32_e32 v67, v67, v66
	s_mov_b32 s4, 0x3db851ec
	v_bfrev_b32_e32 v68, 1
	v_cmp_gt_f32_e32 vcc, s4, v67
	s_movk_i32 s4, 0x3ff
	s_nop 0
	v_cndmask_b32_e32 v67, 0, v68, vcc
	v_mov_b32_e32 v68, 0x21380
	v_and_or_b32 v67, v66, s4, v67
	v_lshl_or_b32 v68, v172, 2, v68
	ds_write_b32 v68, v67
	s_and_b64 exec, exec, vcc
	s_cbranch_execz .LBB0_102
	s_mov_b64 s[6:7], exec
	v_mbcnt_lo_u32_b32 v67, s6, 0
	v_mbcnt_hi_u32_b32 v67, s7, v67
	v_cmp_eq_u32_e32 vcc, 0, v67
	s_and_saveexec_b64 s[4:5], vcc
	s_bcnt1_i32_b64 s6, s[6:7]
	v_mov_b32_e32 v68, 0x21d44
	v_mov_b32_e32 v69, s6
	ds_add_rtn_u32 v68, v68, v69
	s_or_b64 exec, exec, s[4:5]
	s_waitcnt lgkmcnt(0)
	v_readfirstlane_b32 s4, v68
	v_or_b32_e32 v69, 0x1e0, v172
	v_add_f32_e32 v66, 0x3dcccccd, v66
	v_add_lshl_u32 v67, s4, v67, 2
	v_add_u32_e32 v68, 0x21400, v67
	v_add_u32_e32 v67, 0x20400, v67
	ds_write_b32 v68, v69
	ds_write_b32 v67, v66
